# prep histogram and scatter phase-2 loads all issued up front (de-serialized); sections padded to 256B with s_nop
# speedup vs baseline: 1.0077x; 1.0077x over previous
.Lprep_hist_loads:
	s_mov_b64 s[8:9], 0x9000
	v_cmp_gt_u32_e32 vcc, 0x310, v0
	v_lshl_add_u64 v[18:19], v[2:3], 0, s[8:9]
	s_and_saveexec_b64 s[4:5], vcc
	global_load_dword v16, v[18:19], off
	s_or_b64 exec, exec, s[4:5]
	global_load_dword v7, v[2:3], off
	v_lshl_add_u64 v[2:3], v[2:3], 0, s[6:7]
	global_load_dword v8, v[2:3], off
	v_lshl_add_u64 v[2:3], v[2:3], 0, s[6:7]
	global_load_dword v9, v[2:3], off
	v_lshl_add_u64 v[2:3], v[2:3], 0, s[6:7]
	global_load_dword v10, v[2:3], off
	v_lshl_add_u64 v[2:3], v[2:3], 0, s[6:7]
	global_load_dword v11, v[2:3], off
	v_lshl_add_u64 v[2:3], v[2:3], 0, s[6:7]
	global_load_dword v12, v[2:3], off
	v_lshl_add_u64 v[2:3], v[2:3], 0, s[6:7]
	global_load_dword v13, v[2:3], off
	v_lshl_add_u64 v[2:3], v[2:3], 0, s[6:7]
	global_load_dword v14, v[2:3], off
	v_lshl_add_u64 v[2:3], v[2:3], 0, s[6:7]
	global_load_dword v15, v[2:3], off
	s_waitcnt vmcnt(8)
	v_ashrrev_i32_e32 v7, 6, v7
	v_lshlrev_b32_e32 v7, 2, v7
	ds_add_u32 v7, v1
	s_waitcnt vmcnt(7)
	v_ashrrev_i32_e32 v8, 6, v8
	v_lshlrev_b32_e32 v8, 2, v8
	ds_add_u32 v8, v1
	s_waitcnt vmcnt(6)
	v_ashrrev_i32_e32 v9, 6, v9
	v_lshlrev_b32_e32 v9, 2, v9
	ds_add_u32 v9, v1
	s_waitcnt vmcnt(5)
	v_ashrrev_i32_e32 v10, 6, v10
	v_lshlrev_b32_e32 v10, 2, v10
	ds_add_u32 v10, v1
	s_waitcnt vmcnt(4)
	v_ashrrev_i32_e32 v11, 6, v11
	v_lshlrev_b32_e32 v11, 2, v11
	ds_add_u32 v11, v1
	s_waitcnt vmcnt(3)
	v_ashrrev_i32_e32 v12, 6, v12
	v_lshlrev_b32_e32 v12, 2, v12
	ds_add_u32 v12, v1
	s_waitcnt vmcnt(2)
	v_ashrrev_i32_e32 v13, 6, v13
	v_lshlrev_b32_e32 v13, 2, v13
	ds_add_u32 v13, v1
	s_waitcnt vmcnt(1)
	v_ashrrev_i32_e32 v14, 6, v14
	v_lshlrev_b32_e32 v14, 2, v14
	ds_add_u32 v14, v1
	s_waitcnt vmcnt(0)
	v_ashrrev_i32_e32 v15, 6, v15
	v_lshlrev_b32_e32 v15, 2, v15
	ds_add_u32 v15, v1
	s_and_saveexec_b64 s[4:5], vcc
	v_ashrrev_i32_e32 v16, 6, v16
	v_lshlrev_b32_e32 v16, 2, v16
	ds_add_u32 v16, v1
	s_or_b64 exec, exec, s[4:5]
	s_mulk_i32 s2, 0x640
	v_add_u32_e32 v0, s2, v0
	v_mov_b32_e32 v1, 0
	v_lshl_add_u64 v[0:1], v[0:1], 2, s[0:1]
	s_mov_b64 s[0:1], 0
	s_mov_b64 s[2:3], 0x1000
	s_movk_i32 s4, 0x23f
	s_waitcnt lgkmcnt(0)
	s_barrier

.Lscat_loads:
	s_mov_b64 s[16:17], 0x9000
	v_cmp_gt_u32_e32 vcc, 0x310, v0
	v_lshl_add_u64 v[40:41], v[2:3], 0, s[16:17]
	v_lshl_add_u64 v[42:43], v[4:5], 0, s[16:17]
	s_and_saveexec_b64 s[0:1], vcc
	global_load_dword v29, v[40:41], off
	global_load_dword v39, v[42:43], off
	s_or_b64 exec, exec, s[0:1]
	global_load_dword v20, v[2:3], off
	v_lshl_add_u64 v[2:3], v[2:3], 0, s[2:3]
	global_load_dword v21, v[2:3], off
	v_lshl_add_u64 v[2:3], v[2:3], 0, s[2:3]
	global_load_dword v22, v[2:3], off
	v_lshl_add_u64 v[2:3], v[2:3], 0, s[2:3]
	global_load_dword v23, v[2:3], off
	v_lshl_add_u64 v[2:3], v[2:3], 0, s[2:3]
	global_load_dword v24, v[2:3], off
	v_lshl_add_u64 v[2:3], v[2:3], 0, s[2:3]
	global_load_dword v25, v[2:3], off
	v_lshl_add_u64 v[2:3], v[2:3], 0, s[2:3]
	global_load_dword v26, v[2:3], off
	v_lshl_add_u64 v[2:3], v[2:3], 0, s[2:3]
	global_load_dword v27, v[2:3], off
	v_lshl_add_u64 v[2:3], v[2:3], 0, s[2:3]
	global_load_dword v28, v[2:3], off
	global_load_dword v30, v[4:5], off
	v_lshl_add_u64 v[4:5], v[4:5], 0, s[2:3]
	global_load_dword v31, v[4:5], off
	v_lshl_add_u64 v[4:5], v[4:5], 0, s[2:3]
	global_load_dword v32, v[4:5], off
	v_lshl_add_u64 v[4:5], v[4:5], 0, s[2:3]
	global_load_dword v33, v[4:5], off
	v_lshl_add_u64 v[4:5], v[4:5], 0, s[2:3]
	global_load_dword v34, v[4:5], off
	v_lshl_add_u64 v[4:5], v[4:5], 0, s[2:3]
	global_load_dword v35, v[4:5], off
	v_lshl_add_u64 v[4:5], v[4:5], 0, s[2:3]
	global_load_dword v36, v[4:5], off
	v_lshl_add_u64 v[4:5], v[4:5], 0, s[2:3]
	global_load_dword v37, v[4:5], off
	v_lshl_add_u64 v[4:5], v[4:5], 0, s[2:3]
	global_load_dword v38, v[4:5], off
	v_add_u32_e32 v13, s4, v0
	s_waitcnt vmcnt(17)
	v_ashrrev_i32_e32 v50, 6, v20
	v_lshl_add_u32 v60, v50, 2, v1
	ds_add_rtn_u32 v60, v60, v6
	v_lshlrev_b32_e32 v20, 20, v20
	v_mov_b32_e32 v70, v13
	v_and_or_b32 v20, v20, s5, v70
	s_waitcnt vmcnt(16)
	v_ashrrev_i32_e32 v51, 6, v21
	v_lshl_add_u32 v61, v51, 2, v1
	ds_add_rtn_u32 v61, v61, v6
	v_lshlrev_b32_e32 v21, 20, v21
	v_add_u32_e32 v71, 0x400, v13
	v_and_or_b32 v21, v21, s5, v71
	s_waitcnt vmcnt(15)
	v_ashrrev_i32_e32 v52, 6, v22
	v_lshl_add_u32 v62, v52, 2, v1
	ds_add_rtn_u32 v62, v62, v6
	v_lshlrev_b32_e32 v22, 20, v22
	v_add_u32_e32 v72, 0x800, v13
	v_and_or_b32 v22, v22, s5, v72
	s_waitcnt vmcnt(14)
	v_ashrrev_i32_e32 v53, 6, v23
	v_lshl_add_u32 v63, v53, 2, v1
	ds_add_rtn_u32 v63, v63, v6
	v_lshlrev_b32_e32 v23, 20, v23
	v_add_u32_e32 v73, 0xc00, v13
	v_and_or_b32 v23, v23, s5, v73
	s_waitcnt vmcnt(13)
	v_ashrrev_i32_e32 v54, 6, v24
	v_lshl_add_u32 v64, v54, 2, v1
	ds_add_rtn_u32 v64, v64, v6
	v_lshlrev_b32_e32 v24, 20, v24
	v_add_u32_e32 v74, 0x1000, v13
	v_and_or_b32 v24, v24, s5, v74
	s_waitcnt vmcnt(12)
	v_ashrrev_i32_e32 v55, 6, v25
	v_lshl_add_u32 v65, v55, 2, v1
	ds_add_rtn_u32 v65, v65, v6
	v_lshlrev_b32_e32 v25, 20, v25
	v_add_u32_e32 v75, 0x1400, v13
	v_and_or_b32 v25, v25, s5, v75
	s_waitcnt vmcnt(11)
	v_ashrrev_i32_e32 v56, 6, v26
	v_lshl_add_u32 v66, v56, 2, v1
	ds_add_rtn_u32 v66, v66, v6
	v_lshlrev_b32_e32 v26, 20, v26
	v_add_u32_e32 v76, 0x1800, v13
	v_and_or_b32 v26, v26, s5, v76
	s_waitcnt vmcnt(10)
	v_ashrrev_i32_e32 v57, 6, v27
	v_lshl_add_u32 v67, v57, 2, v1
	ds_add_rtn_u32 v67, v67, v6
	v_lshlrev_b32_e32 v27, 20, v27
	v_add_u32_e32 v77, 0x1c00, v13
	v_and_or_b32 v27, v27, s5, v77
	s_waitcnt vmcnt(9)
	v_ashrrev_i32_e32 v58, 6, v28
	v_lshl_add_u32 v68, v58, 2, v1
	ds_add_rtn_u32 v68, v68, v6
	v_lshlrev_b32_e32 v28, 20, v28
	v_add_u32_e32 v78, 0x2000, v13
	v_and_or_b32 v28, v28, s5, v78
	s_and_saveexec_b64 s[0:1], vcc
	v_ashrrev_i32_e32 v59, 6, v29
	v_lshl_add_u32 v69, v59, 2, v1
	ds_add_rtn_u32 v69, v69, v6
	v_lshlrev_b32_e32 v29, 20, v29
	v_add_u32_e32 v79, 0x2400, v13
	v_and_or_b32 v29, v29, s5, v79
	s_or_b64 exec, exec, s[0:1]
	s_waitcnt lgkmcnt(0)
	v_lshlrev_b32_e32 v70, 2, v60
	v_lshl_add_u32 v60, v60, 1, s6
	ds_write_b32 v70, v20
	ds_write_b16 v60, v50
	s_waitcnt vmcnt(8)
	ds_write_b32 v70, v30 offset:40000
	v_lshlrev_b32_e32 v71, 2, v61
	v_lshl_add_u32 v61, v61, 1, s6
	ds_write_b32 v71, v21
	ds_write_b16 v61, v51
	s_waitcnt vmcnt(7)
	ds_write_b32 v71, v31 offset:40000
	v_lshlrev_b32_e32 v72, 2, v62
	v_lshl_add_u32 v62, v62, 1, s6
	ds_write_b32 v72, v22
	ds_write_b16 v62, v52
	s_waitcnt vmcnt(6)
	ds_write_b32 v72, v32 offset:40000
	v_lshlrev_b32_e32 v73, 2, v63
	v_lshl_add_u32 v63, v63, 1, s6
	ds_write_b32 v73, v23
	ds_write_b16 v63, v53
	s_waitcnt vmcnt(5)
	ds_write_b32 v73, v33 offset:40000
	v_lshlrev_b32_e32 v74, 2, v64
	v_lshl_add_u32 v64, v64, 1, s6
	ds_write_b32 v74, v24
	ds_write_b16 v64, v54
	s_waitcnt vmcnt(4)
	ds_write_b32 v74, v34 offset:40000
	v_lshlrev_b32_e32 v75, 2, v65
	v_lshl_add_u32 v65, v65, 1, s6
	ds_write_b32 v75, v25
	ds_write_b16 v65, v55
	s_waitcnt vmcnt(3)
	ds_write_b32 v75, v35 offset:40000
	v_lshlrev_b32_e32 v76, 2, v66
	v_lshl_add_u32 v66, v66, 1, s6
	ds_write_b32 v76, v26
	ds_write_b16 v66, v56
	s_waitcnt vmcnt(2)
	ds_write_b32 v76, v36 offset:40000
	v_lshlrev_b32_e32 v77, 2, v67
	v_lshl_add_u32 v67, v67, 1, s6
	ds_write_b32 v77, v27
	ds_write_b16 v67, v57
	s_waitcnt vmcnt(1)
	ds_write_b32 v77, v37 offset:40000
	v_lshlrev_b32_e32 v78, 2, v68
	v_lshl_add_u32 v68, v68, 1, s6
	ds_write_b32 v78, v28
	ds_write_b16 v68, v58
	s_waitcnt vmcnt(0)
	ds_write_b32 v78, v38 offset:40000
	s_and_saveexec_b64 s[0:1], vcc
	v_lshlrev_b32_e32 v79, 2, v69
	v_lshl_add_u32 v69, v69, 1, s6
	ds_write_b32 v79, v29
	ds_write_b16 v69, v59
	ds_write_b32 v79, v39 offset:40000
	s_or_b64 exec, exec, s[0:1]
	v_add_u32_e32 v1, 0x13880, v10
	v_lshlrev_b32_e32 v2, 2, v0
	s_mov_b64 s[0:1], 0
	s_movk_i32 s2, 0x230f
	s_waitcnt lgkmcnt(0)
	s_barrier

.Lfunc_end4:
	.size	_Z12layer_kernelILb1ELi512ELi64EEvPKDv8_DF16_PKfPS0_PiS6_S6_S2_S4_S5_PfPK15HIP_vector_typeIiLj2EEPKi, .Lfunc_end4-_Z12layer_kernelILb1ELi512ELi64EEvPKDv8_DF16_PKfPS0_PiS6_S6_S2_S4_S5_PfPK15HIP_vector_typeIiLj2EEPKi
	.p2alignl 8, 3212836864
	.set _Z12layer_kernelILb1ELi512ELi64EEvPKDv8_DF16_PKfPS0_PiS6_S6_S2_S4_S5_PfPK15HIP_vector_typeIiLj2EEPKi.num_vgpr, 61
	.set _Z12layer_kernelILb1ELi512ELi64EEvPKDv8_DF16_PKfPS0_PiS6_S6_S2_S4_S5_PfPK15HIP_vector_typeIiLj2EEPKi.num_agpr, 0
	.set _Z12layer_kernelILb1ELi512ELi64EEvPKDv8_DF16_PKfPS0_PiS6_S6_S2_S4_S5_PfPK15HIP_vector_typeIiLj2EEPKi.numbered_sgpr, 46
	.set _Z12layer_kernelILb1ELi512ELi64EEvPKDv8_DF16_PKfPS0_PiS6_S6_S2_S4_S5_PfPK15HIP_vector_typeIiLj2EEPKi.num_named_barrier, 0
	.set _Z12layer_kernelILb1ELi512ELi64EEvPKDv8_DF16_PKfPS0_PiS6_S6_S2_S4_S5_PfPK15HIP_vector_typeIiLj2EEPKi.private_seg_size, 0
	.set _Z12layer_kernelILb1ELi512ELi64EEvPKDv8_DF16_PKfPS0_PiS6_S6_S2_S4_S5_PfPK15HIP_vector_typeIiLj2EEPKi.uses_vcc, 1
	.set _Z12layer_kernelILb1ELi512ELi64EEvPKDv8_DF16_PKfPS0_PiS6_S6_S2_S4_S5_PfPK15HIP_vector_typeIiLj2EEPKi.uses_flat_scratch, 0
	.set _Z12layer_kernelILb1ELi512ELi64EEvPKDv8_DF16_PKfPS0_PiS6_S6_S2_S4_S5_PfPK15HIP_vector_typeIiLj2EEPKi.has_dyn_sized_stack, 0
	.set _Z12layer_kernelILb1ELi512ELi64EEvPKDv8_DF16_PKfPS0_PiS6_S6_S2_S4_S5_PfPK15HIP_vector_typeIiLj2EEPKi.has_recursion, 0
	.set _Z12layer_kernelILb1ELi512ELi64EEvPKDv8_DF16_PKfPS0_PiS6_S6_S2_S4_S5_PfPK15HIP_vector_typeIiLj2EEPKi.has_indirect_call, 0

	.text
	.p2alignl 6, 3212836864
	.fill 256, 4, 3212836864
	.p2alignl 8, 3212836864
